# U2: bias load hoisted to the prologue too (on top of the U3f store-ack wait removal)
# baseline (speedup 1.0000x reference)
_Z4k_U2PKtPK15HIP_vector_typeIjLj4EEPKdPKfS8_S8_PtPd:
	s_load_dwordx2 s[4:5], s[0:1], 0x8
	s_load_dwordx2 s[20:21], s[0:1], 0x0
	s_load_dword s22, s[0:1], 0x40
	s_load_dwordx2 s[24:25], s[0:1], 0x28
	v_mov_b32_e32 v3, 0
	v_lshlrev_b32_e32 v2, 4, v0
	s_movk_i32 s3, 0x1000
	v_lshlrev_b32_e32 v1, 2, v0
	s_waitcnt lgkmcnt(0)
	v_lshrrev_b32_e32 v60, 6, v0
	v_mul_lo_u32 v60, s22, v60
	v_add_u32_e32 v60, s2, v60
	v_min_u32_e32 v60, 0xc34, v60
	v_and_b32_e32 v61, 31, v0
	v_lshl_or_b32 v60, v60, 5, v61
	v_and_b32_e32 v61, 32, v0
	v_lshlrev_b32_e32 v60, 7, v60
	v_lshl_add_u32 v60, v61, 1, v60
	global_load_dwordx4 v[44:47], v60, s[20:21] offset:48
	global_load_dwordx4 v[48:51], v60, s[20:21] offset:32
	global_load_dwordx4 v[52:55], v60, s[20:21] offset:16
	global_load_dwordx4 v[56:59], v60, s[20:21]
	v_and_b32_e32 v61, 31, v0
	v_lshlrev_b32_e32 v61, 3, v61
	global_load_dwordx2 a[0:1], v61, s[24:25]
	v_lshl_add_u64 v[16:17], s[4:5], 0, v[2:3]
	v_add_co_u32_e32 v18, vcc, 0x1000, v16
	global_load_dwordx4 v[4:7], v2, s[4:5]
	s_nop 0
	v_addc_co_u32_e32 v19, vcc, 0, v17, vcc
	v_add_co_u32_e32 v20, vcc, 0x2000, v16
	s_nop 1
	v_addc_co_u32_e32 v21, vcc, 0, v17, vcc
	global_load_dwordx4 v[8:11], v[18:19], off
	global_load_dwordx4 v[12:15], v[20:21], off
	v_add_co_u32_e32 v16, vcc, 0x3000, v16
	s_nop 1
	v_addc_co_u32_e32 v17, vcc, 0, v17, vcc
	global_load_dwordx4 v[16:19], v[16:17], off
	v_cmp_gt_u32_e32 vcc, 64, v0
	s_waitcnt vmcnt(3)
	ds_write_b128 v2, v[4:7]
	s_waitcnt vmcnt(2)
	ds_write_b128 v2, v[8:11] offset:4096
	s_waitcnt vmcnt(1)
	ds_write_b128 v2, v[12:15] offset:8192
	s_waitcnt vmcnt(0)
	ds_write_b128 v2, v[16:19] offset:12288
	s_and_saveexec_b64 s[6:7], vcc
	s_cbranch_execz .LBB3_2
	s_load_dwordx4 s[8:11], s[0:1], 0x10
	s_load_dwordx2 s[4:5], s[0:1], 0x20
	v_lshlrev_b32_e32 v4, 3, v0
	v_mov_b32_e32 v5, 0
	s_mov_b32 s12, 0
	s_waitcnt lgkmcnt(0)
	global_load_dwordx2 v[8:9], v4, s[8:9]
	global_load_dwordx2 v[10:11], v4, s[8:9] offset:512
	global_load_dwordx2 v[12:13], v4, s[8:9] offset:1024
	global_load_dwordx2 v[14:15], v4, s[8:9] offset:1536
	global_load_dwordx2 v[16:17], v4, s[8:9] offset:2048
	global_load_dwordx2 v[18:19], v4, s[8:9] offset:2560
	global_load_dwordx2 v[20:21], v4, s[8:9] offset:3072
	global_load_dwordx2 v[22:23], v4, s[8:9] offset:3584
	v_lshl_add_u64 v[6:7], s[8:9], 0, v[4:5]
	v_add_co_u32_e32 v4, vcc, s3, v6
	s_mov_b32 s8, 0x88e368f1
	s_nop 0
	v_addc_co_u32_e32 v5, vcc, 0, v7, vcc
	global_load_dwordx2 v[6:7], v[4:5], off
	global_load_dwordx2 v[24:25], v[4:5], off offset:512
	global_load_dwordx2 v[26:27], v[4:5], off offset:1024
	global_load_dwordx2 v[28:29], v[4:5], off offset:1536
	global_load_dwordx2 v[30:31], v[4:5], off offset:2048
	global_load_dwordx2 v[32:33], v[4:5], off offset:2560
	global_load_dwordx2 v[34:35], v[4:5], off offset:3072
	global_load_dwordx2 v[36:37], v[4:5], off offset:3584
	global_load_dword v2, v1, s[10:11]
	global_load_dword v38, v1, s[4:5]
	s_mov_b32 s10, 0
	s_mov_b32 s11, 0x40f86a00
	s_mov_b32 s9, 0x3ee4f8b5
	s_brev_b32 s13, 8
	v_mov_b32_e32 v39, 0x100
	v_mov_b32_e32 v40, 0xffffff80
	v_mov_b32_e32 v41, 0x260
	s_waitcnt vmcnt(17)
	v_add_f64 v[4:5], v[8:9], 0
	s_waitcnt vmcnt(16)
	v_add_f64 v[8:9], v[10:11], 0
	s_waitcnt vmcnt(15)
	v_add_f64 v[4:5], v[4:5], v[12:13]
	s_waitcnt vmcnt(14)
	v_add_f64 v[8:9], v[8:9], v[14:15]
	s_waitcnt vmcnt(13)
	v_add_f64 v[4:5], v[4:5], v[16:17]
	s_waitcnt vmcnt(12)
	v_add_f64 v[8:9], v[8:9], v[18:19]
	s_waitcnt vmcnt(11)
	v_add_f64 v[4:5], v[4:5], v[20:21]
	s_waitcnt vmcnt(10)
	v_add_f64 v[8:9], v[8:9], v[22:23]
	s_waitcnt vmcnt(9)
	v_add_f64 v[4:5], v[4:5], v[6:7]
	s_waitcnt vmcnt(8)
	v_add_f64 v[6:7], v[8:9], v[24:25]
	s_waitcnt vmcnt(7)
	v_add_f64 v[4:5], v[4:5], v[26:27]
	s_waitcnt vmcnt(6)
	v_add_f64 v[6:7], v[6:7], v[28:29]
	s_waitcnt vmcnt(5)
	v_add_f64 v[4:5], v[4:5], v[30:31]
	s_waitcnt vmcnt(4)
	v_add_f64 v[6:7], v[6:7], v[32:33]
	s_waitcnt vmcnt(3)
	v_add_f64 v[4:5], v[4:5], v[34:35]
	s_waitcnt vmcnt(2)
	v_add_f64 v[6:7], v[6:7], v[36:37]
	v_div_scale_f64 v[8:9], s[4:5], s[10:11], s[10:11], v[4:5]
	v_div_scale_f64 v[12:13], s[4:5], s[10:11], s[10:11], v[6:7]
	v_rcp_f64_e32 v[14:15], v[8:9]
	v_rcp_f64_e32 v[16:17], v[12:13]
	v_div_scale_f64 v[10:11], vcc, v[4:5], s[10:11], v[4:5]
	v_fma_f64 v[20:21], -v[8:9], v[14:15], 1.0
	v_fma_f64 v[22:23], -v[12:13], v[16:17], 1.0
	v_fmac_f64_e32 v[14:15], v[14:15], v[20:21]
	v_fmac_f64_e32 v[16:17], v[16:17], v[22:23]
	v_fma_f64 v[20:21], -v[8:9], v[14:15], 1.0
	v_fma_f64 v[22:23], -v[12:13], v[16:17], 1.0
	v_fmac_f64_e32 v[14:15], v[14:15], v[20:21]
	v_div_scale_f64 v[18:19], s[4:5], v[6:7], s[10:11], v[6:7]
	v_fmac_f64_e32 v[16:17], v[16:17], v[22:23]
	v_mul_f64 v[20:21], v[10:11], v[14:15]
	v_mul_f64 v[22:23], v[18:19], v[16:17]
	v_fma_f64 v[8:9], -v[8:9], v[20:21], v[10:11]
	v_fma_f64 v[10:11], -v[12:13], v[22:23], v[18:19]
	v_div_fmas_f64 v[8:9], v[8:9], v[14:15], v[20:21]
	s_mov_b64 vcc, s[4:5]
	v_div_fixup_f64 v[4:5], v[8:9], s[10:11], v[4:5]
	v_div_fmas_f64 v[8:9], v[10:11], v[16:17], v[22:23]
	v_div_fixup_f64 v[6:7], v[8:9], s[10:11], v[6:7]
	v_fma_f64 v[6:7], -v[4:5], v[4:5], v[6:7]
	v_cmp_ngt_f64_e32 vcc, 0, v[6:7]
	s_waitcnt vmcnt(1)
	v_cvt_f64_f32_e32 v[10:11], v2
	s_waitcnt vmcnt(0)
	v_cvt_f64_f32_e32 v[12:13], v38
	v_cndmask_b32_e32 v7, 0, v7, vcc
	v_cndmask_b32_e32 v6, 0, v6, vcc
	v_add_f64 v[6:7], v[6:7], s[8:9]
	v_cmp_gt_f64_e32 vcc, s[12:13], v[6:7]
	v_add_f64 v[4:5], v[4:5], 0
	s_nop 0
	v_cndmask_b32_e32 v8, 0, v39, vcc
	v_ldexp_f64 v[6:7], v[6:7], v8
	v_rsq_f64_e32 v[8:9], v[6:7]
	v_cndmask_b32_e32 v2, 0, v40, vcc
	v_cmp_class_f64_e32 vcc, v[6:7], v41
	v_mul_f64 v[14:15], v[6:7], v[8:9]
	v_mul_f64 v[8:9], v[8:9], 0.5
	v_fma_f64 v[16:17], -v[8:9], v[14:15], 0.5
	v_fmac_f64_e32 v[14:15], v[14:15], v[16:17]
	v_fmac_f64_e32 v[8:9], v[8:9], v[16:17]
	v_fma_f64 v[16:17], -v[14:15], v[14:15], v[6:7]
	v_fmac_f64_e32 v[14:15], v[16:17], v[8:9]
	v_fma_f64 v[16:17], -v[14:15], v[14:15], v[6:7]
	v_fmac_f64_e32 v[14:15], v[16:17], v[8:9]
	v_ldexp_f64 v[8:9], v[14:15], v2
	v_cndmask_b32_e32 v7, v9, v7, vcc
	v_cndmask_b32_e32 v6, v8, v6, vcc
	v_div_scale_f64 v[8:9], s[4:5], v[6:7], v[6:7], v[10:11]
	v_rcp_f64_e32 v[14:15], v[8:9]
	v_div_scale_f64 v[16:17], vcc, v[10:11], v[6:7], v[10:11]
	v_fma_f64 v[18:19], -v[8:9], v[14:15], 1.0
	v_fmac_f64_e32 v[14:15], v[14:15], v[18:19]
	v_fma_f64 v[18:19], -v[8:9], v[14:15], 1.0
	v_fmac_f64_e32 v[14:15], v[14:15], v[18:19]
	v_mul_f64 v[18:19], v[16:17], v[14:15]
	v_fma_f64 v[8:9], -v[8:9], v[18:19], v[16:17]
	v_div_fmas_f64 v[8:9], v[8:9], v[14:15], v[18:19]
	v_div_fixup_f64 v[6:7], v[8:9], v[6:7], v[10:11]
	v_fma_f64 v[4:5], -v[4:5], v[6:7], v[12:13]
	v_cvt_f32_f64_e32 v2, v[6:7]
	v_cvt_f32_f64_e32 v4, v[4:5]
	ds_write2st64_b32 v1, v2, v4 offset0:72 offset1:73
.LBB3_2:
	s_or_b64 exec, exec, s[6:7]
	s_waitcnt lgkmcnt(0)
	s_barrier
	s_load_dword s3, s[0:1], 0x40
	v_lshrrev_b32_e32 v17, 6, v0
	v_and_b32_e32 v16, 63, v0
	v_mov_b32_e32 v5, 0
	v_mov_b32_e32 v6, 0
	s_waitcnt lgkmcnt(0)
	v_mul_lo_u32 v2, s3, v17
	v_add_u32_e32 v2, s2, v2
	s_movk_i32 s3, 0xc35
	v_cmp_gt_i32_e32 vcc, s3, v2
	v_mov_b32_e32 v7, 0
	s_and_saveexec_b64 s[8:9], vcc
	s_cbranch_execz .LBB3_4
	s_load_dwordx2 s[4:5], s[0:1], 0x0
	v_and_b32_e32 v18, 31, v0
	v_lshlrev_b32_e32 v19, 5, v2
	v_or_b32_e32 v2, v19, v18
	v_ashrrev_i32_e32 v3, 31, v2
	v_lshlrev_b64 v[2:3], 7, v[2:3]
	v_and_b32_e32 v4, 32, v0
	s_waitcnt lgkmcnt(0)
	v_lshl_add_u64 v[2:3], s[4:5], 0, v[2:3]
	v_lshlrev_b32_e32 v14, 1, v4
	v_mov_b32_e32 v15, 0
	v_lshl_add_u64 v[20:21], v[2:3], 0, v[14:15]
	s_waitcnt vmcnt(0)
	v_mov_b32_e32 v2, v44
	v_mov_b32_e32 v3, v45
	v_mov_b32_e32 v4, v46
	v_mov_b32_e32 v5, v47
	v_mov_b32_e32 v6, v48
	v_mov_b32_e32 v7, v49
	v_mov_b32_e32 v8, v50
	v_mov_b32_e32 v9, v51
	v_mov_b32_e32 v10, v52
	v_mov_b32_e32 v11, v53
	v_mov_b32_e32 v12, v54
	v_mov_b32_e32 v13, v55
	v_mov_b32_e32 v22, v56
	v_mov_b32_e32 v23, v57
	v_mov_b32_e32 v24, v58
	v_mov_b32_e32 v25, v59
	s_load_dwordx4 s[4:7], s[0:1], 0x28
	v_lshlrev_b32_e32 v14, 3, v18
	v_and_b32_e32 v20, 0x80, v1
	s_waitcnt vmcnt(0)
	s_waitcnt lgkmcnt(0)
	v_lshlrev_b32_e32 v21, 16, v22
	v_and_b32_e32 v50, 0xffff0000, v22
	v_lshlrev_b32_e32 v51, 16, v23
	v_and_b32_e32 v46, 0xffff0000, v23
	v_lshlrev_b32_e32 v54, 16, v24
	v_and_b32_e32 v55, 0xffff0000, v24
	v_lshlrev_b32_e32 v56, 16, v25
	v_and_b32_e32 v52, 0xffff0000, v25
	v_lshlrev_b32_e32 v57, 16, v10
	v_and_b32_e32 v58, 0xffff0000, v10
	v_lshlrev_b32_e32 v59, 16, v11
	v_and_b32_e32 v60, 0xffff0000, v11
	v_lshlrev_b32_e32 v61, 16, v12
	v_and_b32_e32 v62, 0xffff0000, v12
	v_lshlrev_b32_e32 v63, 16, v13
	v_and_b32_e32 v64, 0xffff0000, v13
	ds_read_b128 v[10:13], v20 offset:18432
	ds_read_b128 v[22:25], v20 offset:18688
	ds_read_b128 v[26:29], v20 offset:18448
	ds_read_b128 v[30:33], v20 offset:18704
	ds_read_b128 v[34:37], v20 offset:18464
	ds_read_b128 v[38:41], v20 offset:18480
	ds_read_b128 v[42:45], v20 offset:18720
	v_lshlrev_b32_e32 v14, 4, v16
	s_waitcnt lgkmcnt(3)
	v_fmac_f32_e32 v33, v29, v52
	v_lshlrev_b32_e32 v65, 16, v6
	v_fmac_f32_e32 v25, v13, v46
	v_fma_f32 v21, v10, v21, v22
	v_fma_f32 v22, v11, v50, v23
	v_fma_f32 v23, v12, v51, v24
	v_fma_f32 v24, v26, v54, v30
	v_fma_f32 v54, v27, v55, v31
	v_fma_f32 v55, v28, v56, v32
	v_max_f32_e32 v25, 0, v25
	v_max_f32_e32 v21, 0, v21
	v_max_f32_e32 v22, 0, v22
	v_max_f32_e32 v23, 0, v23
	s_waitcnt lgkmcnt(0)
	v_fma_f32 v42, v34, v57, v42
	v_max_f32_e32 v34, 0, v33
	v_cvt_pk_f16_f32 v22, v21, v22
	v_cvt_pk_f16_f32 v23, v23, v25
	v_max_f32_e32 v21, 0, v24
	v_max_f32_e32 v24, 0, v54
	v_max_f32_e32 v25, 0, v55
	ds_read_b128 v[50:53], v14
	ds_read_b128 v[10:13], v14 offset:1024
	v_cvt_pk_f16_f32 v24, v21, v24
	v_cvt_pk_f16_f32 v25, v25, v34
	ds_read_b128 v[26:29], v14 offset:4096
	v_and_b32_e32 v66, 0xffff0000, v6
	v_lshlrev_b32_e32 v67, 16, v7
	v_and_b32_e32 v68, 0xffff0000, v7
	v_lshlrev_b32_e32 v69, 16, v8
	v_and_b32_e32 v70, 0xffff0000, v8
	v_lshlrev_b32_e32 v56, 16, v9
	v_and_b32_e32 v57, 0xffff0000, v9
	ds_read_b128 v[6:9], v14 offset:5120
	ds_read_b128 v[30:33], v14 offset:8192
	ds_read_b128 v[46:49], v20 offset:18736
	v_fmac_f32_e32 v45, v37, v60
	v_fma_f32 v43, v35, v58, v43
	v_fma_f32 v44, v36, v59, v44
	ds_read_b128 v[34:37], v14 offset:9216
	v_lshlrev_b32_e32 v21, 16, v2
	s_waitcnt lgkmcnt(1)
	v_fmac_f32_e32 v49, v41, v64
	v_and_b32_e32 v54, 0xffff0000, v2
	v_fma_f32 v2, v38, v61, v46
	v_fma_f32 v38, v39, v62, v47
	v_fma_f32 v39, v40, v63, v48
	v_lshlrev_b32_e32 v55, 16, v3
	v_and_b32_e32 v58, 0xffff0000, v3
	v_max_f32_e32 v3, 0, v45
	v_max_f32_e32 v40, 0, v42
	v_max_f32_e32 v2, 0, v2
	v_lshlrev_b32_e32 v59, 16, v4
	s_waitcnt vmcnt(0)
	v_accvgpr_mov_b32 a16, a0
	v_accvgpr_mov_b32 a17, a0
	v_accvgpr_mov_b32 a18, a0
	v_accvgpr_mov_b32 a19, a0
	v_accvgpr_mov_b32 a20, a0
	v_accvgpr_mov_b32 a21, a0
	v_accvgpr_mov_b32 a22, a0
	v_accvgpr_mov_b32 a23, a0
	v_accvgpr_mov_b32 a24, a0
	v_accvgpr_mov_b32 a25, a0
	v_accvgpr_mov_b32 a26, a0
	v_accvgpr_mov_b32 a27, a0
	v_accvgpr_mov_b32 a28, a0
	v_accvgpr_mov_b32 a29, a0
	v_accvgpr_mov_b32 a30, a0
	v_accvgpr_mov_b32 a31, a0
	v_accvgpr_mov_b32 a0, a1
	v_accvgpr_mov_b32 a2, a1
	v_mfma_f32_32x32x16_f16 a[16:31], v[22:25], v[50:53], a[16:31]
	v_accvgpr_mov_b32 a3, a1
	v_accvgpr_mov_b32 a4, a1
	v_accvgpr_mov_b32 a5, a1
	v_accvgpr_mov_b32 a6, a1
	v_accvgpr_mov_b32 a7, a1
	v_accvgpr_mov_b32 a8, a1
	v_accvgpr_mov_b32 a9, a1
	v_accvgpr_mov_b32 a10, a1
	v_accvgpr_mov_b32 a11, a1
	v_accvgpr_mov_b32 a12, a1
	v_accvgpr_mov_b32 a13, a1
	v_accvgpr_mov_b32 a14, a1
	v_accvgpr_mov_b32 a15, a1
	ds_read_b128 v[50:53], v14 offset:12288
	v_mfma_f32_32x32x16_f16 a[16:31], v[22:25], v[30:33], a[16:31]
	v_max_f32_e32 v30, 0, v43
	v_max_f32_e32 v31, 0, v44
	v_max_f32_e32 v32, 0, v38
	v_max_f32_e32 v33, 0, v39
	v_max_f32_e32 v38, 0, v49
	v_cvt_pk_f16_f32 v30, v40, v30
	v_cvt_pk_f16_f32 v31, v31, v3
	v_mfma_f32_32x32x16_f16 a[0:15], v[22:25], v[26:29], a[0:15]
	ds_read_b128 v[26:29], v14 offset:13312
	v_cvt_pk_f16_f32 v32, v2, v32
	v_cvt_pk_f16_f32 v33, v33, v38
	s_waitcnt lgkmcnt(1)
	v_mfma_f32_32x32x16_f16 a[0:15], v[22:25], v[50:53], a[0:15]
	ds_read_b128 v[22:25], v20 offset:18752
	ds_read_b128 v[38:41], v20 offset:18496
	ds_read_b128 v[42:45], v20 offset:18512
	ds_read_b128 v[46:49], v20 offset:18768
	v_and_b32_e32 v50, 0xffff0000, v4
	v_lshlrev_b32_e32 v51, 16, v5
	v_and_b32_e32 v52, 0xffff0000, v5
	s_waitcnt lgkmcnt(2)
	v_fma_f32 v2, v38, v65, v22
	v_fma_f32 v3, v39, v66, v23
	v_fma_f32 v4, v40, v67, v24
	v_mfma_f32_32x32x16_f16 a[16:31], v[30:33], v[10:13], a[16:31]
	v_fmac_f32_e32 v25, v41, v68
	s_waitcnt lgkmcnt(0)
	v_fma_f32 v5, v42, v69, v46
	v_fmac_f32_e32 v49, v45, v57
	v_max_f32_e32 v2, 0, v2
	v_max_f32_e32 v3, 0, v3
	v_max_f32_e32 v4, 0, v4
	v_max_f32_e32 v5, 0, v5
	v_mfma_f32_32x32x16_f16 a[0:15], v[30:33], v[6:9], a[0:15]
	v_fma_f32 v6, v43, v70, v47
	v_fma_f32 v7, v44, v56, v48
	v_max_f32_e32 v8, 0, v25
	v_max_f32_e32 v6, 0, v6
	v_max_f32_e32 v7, 0, v7
	v_max_f32_e32 v9, 0, v49
	ds_read_b128 v[10:13], v14 offset:2048
	v_mfma_f32_32x32x16_f16 a[16:31], v[30:33], v[34:37], a[16:31]
	v_cvt_pk_f16_f32 v2, v2, v3
	v_cvt_pk_f16_f32 v3, v4, v8
	v_cvt_pk_f16_f32 v4, v5, v6
	v_cvt_pk_f16_f32 v5, v7, v9
	v_mfma_f32_32x32x16_f16 a[0:15], v[30:33], v[26:29], a[0:15]
	ds_read_b128 v[6:9], v14 offset:3072
	ds_read_b128 v[22:25], v20 offset:18528
	ds_read_b128 v[26:29], v20 offset:18544
	ds_read_b128 v[30:33], v20 offset:18784
	s_waitcnt lgkmcnt(0)
	v_fmac_f32_e32 v33, v25, v58
	v_mfma_f32_32x32x16_f16 a[16:31], v[2:5], v[10:13], a[16:31]
	ds_read_b128 v[10:13], v14 offset:6144
	ds_read_b128 v[34:37], v20 offset:18800
	ds_read_b128 v[38:41], v14 offset:10240
	ds_read_b128 v[42:45], v14 offset:14336
	v_fma_f32 v20, v22, v21, v30
	v_fma_f32 v21, v23, v54, v31
	v_fma_f32 v22, v24, v55, v32
	s_waitcnt lgkmcnt(2)
	v_fmac_f32_e32 v37, v29, v52
	v_mfma_f32_32x32x16_f16 a[0:15], v[2:5], v[10:13], a[0:15]
	v_fma_f32 v10, v26, v59, v34
	v_fma_f32 v11, v27, v50, v35
	v_fma_f32 v12, v28, v51, v36
	v_max_f32_e32 v13, 0, v20
	v_max_f32_e32 v20, 0, v21
	v_max_f32_e32 v21, 0, v22
	v_max_f32_e32 v22, 0, v33
	s_waitcnt lgkmcnt(1)
	v_mfma_f32_32x32x16_f16 a[16:31], v[2:5], v[38:41], a[16:31]
	v_max_f32_e32 v23, 0, v10
	v_max_f32_e32 v24, 0, v11
	v_max_f32_e32 v25, 0, v12
	v_max_f32_e32 v26, 0, v37
	v_cvt_pk_f16_f32 v10, v13, v20
	v_cvt_pk_f16_f32 v11, v21, v22
	v_cvt_pk_f16_f32 v12, v23, v24
	s_waitcnt lgkmcnt(0)
	v_mfma_f32_32x32x16_f16 a[0:15], v[2:5], v[42:45], a[0:15]
	v_cvt_pk_f16_f32 v13, v25, v26
	ds_read_b128 v[2:5], v14 offset:7168
	s_nop 0
	v_mfma_f32_32x32x16_f16 a[16:31], v[10:13], v[6:9], a[16:31]
	s_waitcnt lgkmcnt(0)
	v_mfma_f32_32x32x16_f16 a[0:15], v[10:13], v[2:5], a[0:15]
	ds_read_b128 v[2:5], v14 offset:11264
	s_waitcnt lgkmcnt(0)
	v_mfma_f32_32x32x16_f16 a[16:31], v[10:13], v[2:5], a[16:31]
	ds_read_b128 v[2:5], v14 offset:15360
	v_lshrrev_b32_e32 v14, 3, v0
	v_and_or_b32 v40, v14, 4, v19
	v_lshlrev_b32_e32 v14, 2, v18
	v_ashrrev_i32_e32 v41, 31, v40
	v_lshl_add_u64 v[14:15], s[6:7], 0, v[14:15]
	s_waitcnt lgkmcnt(0)
	v_mfma_f32_32x32x16_f16 a[0:15], v[10:13], v[2:5], a[0:15]
	s_nop 3
	v_accvgpr_read_b32 v19, a16
	v_accvgpr_read_b32 v38, a16
	v_accvgpr_read_b32 v36, a17
	v_accvgpr_read_b32 v34, a18
	v_accvgpr_read_b32 v32, a19
	v_accvgpr_read_b32 v30, a20
	v_accvgpr_read_b32 v28, a21
	v_accvgpr_read_b32 v26, a22
	v_accvgpr_read_b32 v18, a0
	v_cvt_pk_bf16_f32 v42, v19, v18
	v_lshlrev_b64 v[18:19], 7, v[40:41]
	v_lshl_add_u64 v[18:19], v[14:15], 0, v[18:19]
	global_store_dword v[18:19], v42, off
	v_accvgpr_read_b32 v18, a1
	v_accvgpr_read_b32 v19, a17
	v_cvt_pk_bf16_f32 v41, v19, v18
	v_or_b32_e32 v18, 1, v40
	v_ashrrev_i32_e32 v19, 31, v18
	v_lshlrev_b64 v[18:19], 7, v[18:19]
	v_lshl_add_u64 v[18:19], v[14:15], 0, v[18:19]
	global_store_dword v[18:19], v41, off
	v_accvgpr_read_b32 v18, a2
	v_accvgpr_read_b32 v19, a18
	v_cvt_pk_bf16_f32 v41, v19, v18
	v_or_b32_e32 v18, 2, v40
	v_ashrrev_i32_e32 v19, 31, v18
	v_lshlrev_b64 v[18:19], 7, v[18:19]
	v_lshl_add_u64 v[18:19], v[14:15], 0, v[18:19]
	global_store_dword v[18:19], v41, off
	v_accvgpr_read_b32 v18, a3
	v_accvgpr_read_b32 v19, a19
	v_cvt_pk_bf16_f32 v41, v19, v18
	v_or_b32_e32 v18, 3, v40
	v_ashrrev_i32_e32 v19, 31, v18
	v_lshlrev_b64 v[18:19], 7, v[18:19]
	v_lshl_add_u64 v[18:19], v[14:15], 0, v[18:19]
	global_store_dword v[18:19], v41, off
	v_accvgpr_read_b32 v18, a4
	v_accvgpr_read_b32 v19, a20
	v_cvt_pk_bf16_f32 v41, v19, v18
	v_or_b32_e32 v18, 8, v40
	v_ashrrev_i32_e32 v19, 31, v18
	v_lshlrev_b64 v[18:19], 7, v[18:19]
	v_lshl_add_u64 v[18:19], v[14:15], 0, v[18:19]
	global_store_dword v[18:19], v41, off
	v_accvgpr_read_b32 v18, a5
	v_accvgpr_read_b32 v19, a21
	v_cvt_pk_bf16_f32 v41, v19, v18
	v_or_b32_e32 v18, 9, v40
	v_ashrrev_i32_e32 v19, 31, v18
	v_lshlrev_b64 v[18:19], 7, v[18:19]
	v_lshl_add_u64 v[18:19], v[14:15], 0, v[18:19]
	global_store_dword v[18:19], v41, off
	v_accvgpr_read_b32 v18, a6
	v_accvgpr_read_b32 v19, a22
	v_cvt_pk_bf16_f32 v41, v19, v18
	v_or_b32_e32 v18, 10, v40
	v_ashrrev_i32_e32 v19, 31, v18
	v_lshlrev_b64 v[18:19], 7, v[18:19]
	v_lshl_add_u64 v[18:19], v[14:15], 0, v[18:19]
	global_store_dword v[18:19], v41, off
	v_accvgpr_read_b32 v18, a7
	v_accvgpr_read_b32 v19, a23
	v_cvt_pk_bf16_f32 v41, v19, v18
	v_or_b32_e32 v18, 11, v40
	v_ashrrev_i32_e32 v19, 31, v18
	v_lshlrev_b64 v[18:19], 7, v[18:19]
	v_lshl_add_u64 v[18:19], v[14:15], 0, v[18:19]
	global_store_dword v[18:19], v41, off
	v_accvgpr_read_b32 v18, a8
	v_accvgpr_read_b32 v19, a24
	v_cvt_pk_bf16_f32 v41, v19, v18
	v_or_b32_e32 v18, 16, v40
	v_ashrrev_i32_e32 v19, 31, v18
	v_lshlrev_b64 v[18:19], 7, v[18:19]
	v_lshl_add_u64 v[18:19], v[14:15], 0, v[18:19]
	global_store_dword v[18:19], v41, off
	v_accvgpr_read_b32 v18, a9
	v_accvgpr_read_b32 v19, a25
	v_cvt_pk_bf16_f32 v41, v19, v18
	v_or_b32_e32 v18, 17, v40
	v_ashrrev_i32_e32 v19, 31, v18
	v_lshlrev_b64 v[18:19], 7, v[18:19]
	v_lshl_add_u64 v[18:19], v[14:15], 0, v[18:19]
	global_store_dword v[18:19], v41, off
	v_accvgpr_read_b32 v18, a10
	v_accvgpr_read_b32 v19, a26
	v_cvt_pk_bf16_f32 v41, v19, v18
	v_or_b32_e32 v18, 18, v40
	v_ashrrev_i32_e32 v19, 31, v18
	v_lshlrev_b64 v[18:19], 7, v[18:19]
	v_lshl_add_u64 v[18:19], v[14:15], 0, v[18:19]
	global_store_dword v[18:19], v41, off
	v_accvgpr_read_b32 v18, a11
	v_accvgpr_read_b32 v19, a27
	v_cvt_pk_bf16_f32 v41, v19, v18
	v_or_b32_e32 v18, 19, v40
	v_ashrrev_i32_e32 v19, 31, v18
	v_lshlrev_b64 v[18:19], 7, v[18:19]
	v_lshl_add_u64 v[18:19], v[14:15], 0, v[18:19]
	global_store_dword v[18:19], v41, off
	v_accvgpr_read_b32 v18, a12
	v_accvgpr_read_b32 v19, a28
	v_cvt_pk_bf16_f32 v41, v19, v18
	v_or_b32_e32 v18, 24, v40
	v_ashrrev_i32_e32 v19, 31, v18
	v_lshlrev_b64 v[18:19], 7, v[18:19]
	v_lshl_add_u64 v[18:19], v[14:15], 0, v[18:19]
	global_store_dword v[18:19], v41, off
	v_accvgpr_read_b32 v18, a13
	v_accvgpr_read_b32 v19, a29
	v_cvt_pk_bf16_f32 v41, v19, v18
	v_or_b32_e32 v18, 25, v40
	v_ashrrev_i32_e32 v19, 31, v18
	v_lshlrev_b64 v[18:19], 7, v[18:19]
	v_lshl_add_u64 v[18:19], v[14:15], 0, v[18:19]
	global_store_dword v[18:19], v41, off
	v_accvgpr_read_b32 v18, a14
	v_accvgpr_read_b32 v19, a30
	v_cvt_pk_bf16_f32 v41, v19, v18
	v_or_b32_e32 v18, 26, v40
	v_ashrrev_i32_e32 v19, 31, v18
	v_lshlrev_b64 v[18:19], 7, v[18:19]
	v_lshl_add_u64 v[18:19], v[14:15], 0, v[18:19]
	global_store_dword v[18:19], v41, off
	v_accvgpr_read_b32 v18, a15
	v_accvgpr_read_b32 v19, a31
	v_cvt_pk_bf16_f32 v41, v19, v18
	v_or_b32_e32 v18, 27, v40
	v_ashrrev_i32_e32 v19, 31, v18
	v_lshlrev_b64 v[18:19], 7, v[18:19]
	v_accvgpr_read_b32 v39, a0
	v_lshl_add_u64 v[14:15], v[14:15], 0, v[18:19]
	v_accvgpr_read_b32 v37, a1
	global_store_dword v[14:15], v41, off
	v_pk_add_f32 v[14:15], v[38:39], 0 op_sel_hi:[1,0]
	v_accvgpr_read_b32 v35, a2
	v_pk_add_f32 v[14:15], v[14:15], v[36:37]
	v_pk_fma_f32 v[18:19], v[38:39], v[38:39], 0 op_sel_hi:[1,1,0]
	v_accvgpr_read_b32 v33, a3
	v_pk_add_f32 v[14:15], v[14:15], v[34:35]
	v_pk_fma_f32 v[18:19], v[36:37], v[36:37], v[18:19]
	v_accvgpr_read_b32 v31, a4
	v_pk_add_f32 v[14:15], v[14:15], v[32:33]
	v_pk_fma_f32 v[18:19], v[34:35], v[34:35], v[18:19]
	v_accvgpr_read_b32 v29, a5
	v_pk_add_f32 v[14:15], v[14:15], v[30:31]
	v_pk_fma_f32 v[18:19], v[32:33], v[32:33], v[18:19]
	v_accvgpr_read_b32 v27, a6
	v_pk_add_f32 v[14:15], v[14:15], v[28:29]
	v_pk_fma_f32 v[18:19], v[30:31], v[30:31], v[18:19]
	v_accvgpr_read_b32 v24, a23
	v_accvgpr_read_b32 v25, a7
	v_pk_add_f32 v[14:15], v[14:15], v[26:27]
	v_pk_fma_f32 v[18:19], v[28:29], v[28:29], v[18:19]
	v_accvgpr_read_b32 v22, a24
	v_accvgpr_read_b32 v23, a8
	v_pk_fma_f32 v[18:19], v[26:27], v[26:27], v[18:19]
	v_pk_add_f32 v[14:15], v[14:15], v[24:25]
	v_accvgpr_read_b32 v20, a25
	v_accvgpr_read_b32 v21, a9
	v_pk_add_f32 v[14:15], v[14:15], v[22:23]
	v_pk_fma_f32 v[18:19], v[24:25], v[24:25], v[18:19]
	v_accvgpr_read_b32 v12, a26
	v_accvgpr_read_b32 v13, a10
	v_pk_add_f32 v[14:15], v[14:15], v[20:21]
	v_pk_fma_f32 v[18:19], v[22:23], v[22:23], v[18:19]
	v_accvgpr_read_b32 v10, a27
	v_accvgpr_read_b32 v11, a11
	v_pk_add_f32 v[14:15], v[14:15], v[12:13]
	v_pk_fma_f32 v[18:19], v[20:21], v[20:21], v[18:19]
	v_accvgpr_read_b32 v8, a28
	v_accvgpr_read_b32 v9, a12
	v_pk_add_f32 v[14:15], v[14:15], v[10:11]
	v_pk_fma_f32 v[12:13], v[12:13], v[12:13], v[18:19]
	v_accvgpr_read_b32 v6, a29
	v_accvgpr_read_b32 v7, a13
	v_pk_add_f32 v[14:15], v[14:15], v[8:9]
	v_pk_fma_f32 v[10:11], v[10:11], v[10:11], v[12:13]
	v_accvgpr_read_b32 v4, a30
	v_accvgpr_read_b32 v5, a14
	v_pk_add_f32 v[14:15], v[14:15], v[6:7]
	v_pk_fma_f32 v[8:9], v[8:9], v[8:9], v[10:11]
	v_accvgpr_read_b32 v2, a31
	v_accvgpr_read_b32 v3, a15
	v_pk_add_f32 v[14:15], v[14:15], v[4:5]
	v_pk_fma_f32 v[6:7], v[6:7], v[6:7], v[8:9]
	s_nop 0
	v_pk_fma_f32 v[6:7], v[4:5], v[4:5], v[6:7]
	v_pk_add_f32 v[4:5], v[14:15], v[2:3]
	v_pk_fma_f32 v[6:7], v[2:3], v[2:3], v[6:7]
	v_mov_b32_e32 v3, v4
